# ml_gates wave-0 prefix sum (mlstate and mlout): 6 ds_bpermute round trips replaced by the DPP wave scan (row_shr 1/2/4/8, row_bcast 15/31); padded so later code keeps its addresses; on top of v9
# baseline (speedup 1.0000x reference)
.LBB0_734:
	s_or_b64 exec, exec, s[0:1]
	s_andn2_b64 vcc, exec, s[6:7]
	s_waitcnt lgkmcnt(0)
	s_barrier
	s_cbranch_vccnz .LBB0_736
	ds_read_b64 v[2:3], v47 offset:34816
	s_waitcnt lgkmcnt(0)
	v_pk_add_f32 v[4:5], v[2:3], v[2:3] op_sel:[0,1] op_sel_hi:[1,0]
	v_mov_b32_e32 v3, v4
	s_nop 1
	v_add_f32_dpp v3, v3, v3 row_shr:1 row_mask:0xf bank_mask:0xf bound_ctrl:1
	s_nop 1
	v_add_f32_dpp v3, v3, v3 row_shr:2 row_mask:0xf bank_mask:0xf bound_ctrl:1
	s_nop 1
	v_add_f32_dpp v3, v3, v3 row_shr:4 row_mask:0xf bank_mask:0xf bound_ctrl:1
	s_nop 1
	v_add_f32_dpp v3, v3, v3 row_shr:8 row_mask:0xf bank_mask:0xf bound_ctrl:1
	s_nop 1
	v_add_f32_dpp v3, v3, v3 row_bcast:15 row_mask:0xa bank_mask:0xf
	s_nop 1
	v_add_f32_dpp v3, v3, v3 row_bcast:31 row_mask:0xc bank_mask:0xf
	s_branch GSCAN_END0
	s_nop 0
	s_nop 0
	s_nop 0
	s_nop 0
	s_nop 0
	s_nop 0
	s_nop 0
	s_nop 0
	s_nop 0
	s_nop 0
	s_nop 0
	s_nop 0
	s_nop 0
	s_nop 0
	s_nop 0
	s_nop 0
	s_nop 0
	s_nop 0
	s_nop 0
	s_nop 0
	s_nop 0
	s_nop 0
	s_nop 0
	s_nop 0
	s_nop 0
	s_nop 0
	s_nop 0
	s_nop 0
	s_nop 0
	s_nop 0
	s_nop 0
	s_nop 0
	s_nop 0
	s_nop 0
	s_nop 0
	s_nop 0
	s_nop 0
	s_nop 0
	s_nop 0
	s_nop 0
	s_nop 0
	s_nop 0
	s_nop 0
	s_nop 0
	s_nop 0
	s_nop 0
GSCAN_END0:
	v_sub_f32_e32 v6, v3, v4
	v_mov_b32_e32 v3, v4
	v_pk_add_f32 v[2:3], v[2:3], v[6:7] op_sel_hi:[1,0]
	ds_write_b64 v47, v[2:3] offset:34816

.LBB0_1180:
	s_or_b64 exec, exec, s[0:1]
	s_andn2_b64 vcc, exec, s[92:93]
	s_waitcnt lgkmcnt(0)
	s_barrier
	s_cbranch_vccnz .LBB0_1182
	ds_read_b64 v[6:7], v115
	s_waitcnt lgkmcnt(0)
	v_pk_add_f32 v[8:9], v[6:7], v[6:7] op_sel:[0,1] op_sel_hi:[1,0]
	v_mov_b32_e32 v7, v8
	s_nop 1
	v_add_f32_dpp v7, v7, v7 row_shr:1 row_mask:0xf bank_mask:0xf bound_ctrl:1
	s_nop 1
	v_add_f32_dpp v7, v7, v7 row_shr:2 row_mask:0xf bank_mask:0xf bound_ctrl:1
	s_nop 1
	v_add_f32_dpp v7, v7, v7 row_shr:4 row_mask:0xf bank_mask:0xf bound_ctrl:1
	s_nop 1
	v_add_f32_dpp v7, v7, v7 row_shr:8 row_mask:0xf bank_mask:0xf bound_ctrl:1
	s_nop 1
	v_add_f32_dpp v7, v7, v7 row_bcast:15 row_mask:0xa bank_mask:0xf
	s_nop 1
	v_add_f32_dpp v7, v7, v7 row_bcast:31 row_mask:0xc bank_mask:0xf
	s_branch GSCAN_END1
	s_nop 0
	s_nop 0
	s_nop 0
	s_nop 0
	s_nop 0
	s_nop 0
	s_nop 0
	s_nop 0
	s_nop 0
	s_nop 0
	s_nop 0
	s_nop 0
	s_nop 0
	s_nop 0
	s_nop 0
	s_nop 0
	s_nop 0
	s_nop 0
	s_nop 0
	s_nop 0
	s_nop 0
	s_nop 0
	s_nop 0
	s_nop 0
	s_nop 0
	s_nop 0
	s_nop 0
	s_nop 0
	s_nop 0
	s_nop 0
	s_nop 0
	s_nop 0
	s_nop 0
	s_nop 0
	s_nop 0
	s_nop 0
	s_nop 0
	s_nop 0
	s_nop 0
	s_nop 0
	s_nop 0
	s_nop 0
	s_nop 0
	s_nop 0
	s_nop 0
	s_nop 0
GSCAN_END1:
	v_sub_f32_e32 v10, v7, v8
	v_mov_b32_e32 v7, v8
	v_pk_add_f32 v[6:7], v[6:7], v[10:11] op_sel_hi:[1,0]
	ds_write_b64 v115, v[6:7]
